# in-projection K loop: second LDS-DMA piece of phases 1 and 5 issued in phases 4 and 8, counted waits adjusted (on top of v21)
# baseline (speedup 1.0000x reference)
.LBB0_301:
	s_waitcnt vmcnt(7)
	ds_read_b128 v[106:109], v213
	ds_read_b128 v[110:113], v213 offset:1024
	ds_read_b128 v[126:129], v213 offset:2048
	ds_read_b128 v[130:133], v213 offset:3072
	s_add_u32 s68, s66, 0xfff80080
	s_addc_u32 s69, s67, -1
	s_cmp_eq_u32 s94, 28
	s_cselect_b32 s71, s11, s69
	s_cselect_b32 s70, s16, s68
	s_cselect_b32 s69, s57, s93
	s_cselect_b32 s68, s59, s92
	s_add_i32 m0, s65, 0xc000
	ds_read_b128 v[146:149], v214
	ds_read_b128 v[178:181], v214 offset:1024
	ds_read_b128 v[182:185], v214 offset:2048
	ds_read_b128 v[186:189], v214 offset:3072
	ds_read_b128 v[190:193], v214 offset:4096
	ds_read_b128 v[194:197], v214 offset:5120
	ds_read_b128 v[198:201], v214 offset:6144
	ds_read_b128 v[220:223], v214 offset:7168
	global_load_lds_dwordx4 v170, s[66:67]
	s_waitcnt lgkmcnt(8)
	s_barrier
	s_waitcnt lgkmcnt(0)
	s_setprio 1
	s_waitcnt lgkmcnt(0)
	v_mfma_i32_16x16x64_i8 v[142:145], v[106:109], v[146:149], v[142:145]
	v_mfma_i32_16x16x64_i8 v[138:141], v[126:129], v[146:149], v[138:141]
	v_mfma_i32_16x16x64_i8 v[118:121], v[106:109], v[182:185], v[118:121]
	v_mfma_i32_16x16x64_i8 v[114:117], v[126:129], v[182:185], v[114:117]
	v_mfma_i32_16x16x64_i8 v[94:97], v[106:109], v[190:193], v[94:97]
	v_mfma_i32_16x16x64_i8 v[90:93], v[126:129], v[190:193], v[90:93]
	v_mfma_i32_16x16x64_i8 v[78:81], v[106:109], v[198:201], v[78:81]
	v_mfma_i32_16x16x64_i8 v[74:77], v[126:129], v[198:201], v[74:77]
	v_mfma_i32_16x16x64_i8 v[142:145], v[110:113], v[178:181], v[142:145]
	v_mfma_i32_16x16x64_i8 v[138:141], v[130:133], v[178:181], v[138:141]
	v_mfma_i32_16x16x64_i8 v[118:121], v[110:113], v[186:189], v[118:121]
	v_mfma_i32_16x16x64_i8 v[114:117], v[130:133], v[186:189], v[114:117]
	v_mfma_i32_16x16x64_i8 v[94:97], v[110:113], v[194:197], v[94:97]
	v_mfma_i32_16x16x64_i8 v[90:93], v[130:133], v[194:197], v[90:93]
	v_mfma_i32_16x16x64_i8 v[78:81], v[110:113], v[220:223], v[78:81]
	v_mfma_i32_16x16x64_i8 v[74:77], v[130:133], v[220:223], v[74:77]
	s_setprio 0
	s_barrier
	s_add_i32 s95, s89, s75
	s_mov_b32 m0, s95
	ds_read_b128 v[224:227], v215
	ds_read_b128 v[228:231], v215 offset:1024
	ds_read_b128 v[232:235], v215 offset:2048
	ds_read_b128 v[236:239], v215 offset:3072
	global_load_lds_dwordx4 v152, s[68:69]
	s_add_i32 m0, s95, 0x2000
	s_nop 0
	global_load_lds_dwordx4 v156, s[68:69]
	s_waitcnt vmcnt(3)
	s_barrier
	s_waitcnt lgkmcnt(0)
	s_setprio 1
	s_waitcnt lgkmcnt(0)
	v_mfma_i32_16x16x64_i8 v[134:137], v[224:227], v[146:149], v[134:137]
	v_mfma_i32_16x16x64_i8 v[122:125], v[232:235], v[146:149], v[122:125]
	v_mfma_i32_16x16x64_i8 v[102:105], v[224:227], v[182:185], v[102:105]
	v_mfma_i32_16x16x64_i8 v[98:101], v[232:235], v[182:185], v[98:101]
	v_mfma_i32_16x16x64_i8 v[86:89], v[224:227], v[190:193], v[86:89]
	v_mfma_i32_16x16x64_i8 v[82:85], v[232:235], v[190:193], v[82:85]
	v_mfma_i32_16x16x64_i8 v[70:73], v[224:227], v[198:201], v[70:73]
	v_mfma_i32_16x16x64_i8 v[66:69], v[232:235], v[198:201], v[66:69]
	v_mfma_i32_16x16x64_i8 v[134:137], v[228:231], v[178:181], v[134:137]
	v_mfma_i32_16x16x64_i8 v[122:125], v[236:239], v[178:181], v[122:125]
	v_mfma_i32_16x16x64_i8 v[102:105], v[228:231], v[186:189], v[102:105]
	v_mfma_i32_16x16x64_i8 v[98:101], v[236:239], v[186:189], v[98:101]
	v_mfma_i32_16x16x64_i8 v[86:89], v[228:231], v[194:197], v[86:89]
	v_mfma_i32_16x16x64_i8 v[82:85], v[236:239], v[194:197], v[82:85]
	v_mfma_i32_16x16x64_i8 v[70:73], v[228:231], v[220:223], v[70:73]
	v_mfma_i32_16x16x64_i8 v[66:69], v[236:239], v[220:223], v[66:69]
	s_setprio 0
	s_mov_b32 m0, s65
	s_add_u32 s98, s70, 0x80
	s_addc_u32 s99, s71, 0
	s_barrier
	ds_read_b128 v[146:149], v214 offset:16384
	ds_read_b128 v[178:181], v214 offset:17408
	ds_read_b128 v[182:185], v214 offset:18432
	ds_read_b128 v[186:189], v214 offset:19456
	ds_read_b128 v[190:193], v214 offset:20480
	ds_read_b128 v[194:197], v214 offset:21504
	ds_read_b128 v[198:201], v214 offset:22528
	ds_read_b128 v[220:223], v214 offset:23552
	global_load_lds_dwordx4 v150, s[70:71]
	s_mov_b32 m0, s76
	s_nop 0
	global_load_lds_dwordx4 v154, s[70:71]
	s_barrier
	s_waitcnt lgkmcnt(0)
	s_setprio 1
	s_waitcnt lgkmcnt(0)
	v_mfma_i32_16x16x64_i8 v[62:65], v[106:109], v[146:149], v[62:65]
	v_mfma_i32_16x16x64_i8 v[58:61], v[126:129], v[146:149], v[58:61]
	v_mfma_i32_16x16x64_i8 v[46:49], v[106:109], v[182:185], v[46:49]
	v_mfma_i32_16x16x64_i8 v[42:45], v[126:129], v[182:185], v[42:45]
	v_mfma_i32_16x16x64_i8 v[30:33], v[106:109], v[190:193], v[30:33]
	v_mfma_i32_16x16x64_i8 v[26:29], v[126:129], v[190:193], v[26:29]
	v_mfma_i32_16x16x64_i8 v[14:17], v[106:109], v[198:201], v[14:17]
	v_mfma_i32_16x16x64_i8 v[10:13], v[126:129], v[198:201], v[10:13]
	v_mfma_i32_16x16x64_i8 v[62:65], v[110:113], v[178:181], v[62:65]
	v_mfma_i32_16x16x64_i8 v[58:61], v[130:133], v[178:181], v[58:61]
	v_mfma_i32_16x16x64_i8 v[46:49], v[110:113], v[186:189], v[46:49]
	v_mfma_i32_16x16x64_i8 v[42:45], v[130:133], v[186:189], v[42:45]
	v_mfma_i32_16x16x64_i8 v[30:33], v[110:113], v[194:197], v[30:33]
	v_mfma_i32_16x16x64_i8 v[26:29], v[130:133], v[194:197], v[26:29]
	v_mfma_i32_16x16x64_i8 v[14:17], v[110:113], v[220:223], v[14:17]
	v_mfma_i32_16x16x64_i8 v[10:13], v[130:133], v[220:223], v[10:13]
	s_setprio 0
	s_barrier
	s_add_u32 s96, s68, 0x80000
	s_addc_u32 s97, s69, 0
	s_add_i32 s95, s90, s75
	s_mov_b32 m0, s95
	s_nop 0
	global_load_lds_dwordx4 v152, s[96:97]
	s_add_i32 m0, s95, 0x2000
	s_nop 0
	global_load_lds_dwordx4 v156, s[96:97]
	s_add_i32 m0, s65, 0xe000
	s_nop 0
	global_load_lds_dwordx4 v172, s[66:67]
	s_waitcnt vmcnt(7)
	s_barrier
	s_setprio 1
	v_mfma_i32_16x16x64_i8 v[54:57], v[224:227], v[146:149], v[54:57]
	v_mfma_i32_16x16x64_i8 v[50:53], v[232:235], v[146:149], v[50:53]
	v_mfma_i32_16x16x64_i8 v[38:41], v[224:227], v[182:185], v[38:41]
	v_mfma_i32_16x16x64_i8 v[34:37], v[232:235], v[182:185], v[34:37]
	v_mfma_i32_16x16x64_i8 v[22:25], v[224:227], v[190:193], v[22:25]
	v_mfma_i32_16x16x64_i8 v[18:21], v[232:235], v[190:193], v[18:21]
	v_mfma_i32_16x16x64_i8 v[6:9], v[224:227], v[198:201], v[6:9]
	v_mfma_i32_16x16x64_i8 v[2:5], v[232:235], v[198:201], v[2:5]
	v_mfma_i32_16x16x64_i8 v[54:57], v[228:231], v[178:181], v[54:57]
	v_mfma_i32_16x16x64_i8 v[50:53], v[236:239], v[178:181], v[50:53]
	v_mfma_i32_16x16x64_i8 v[38:41], v[228:231], v[186:189], v[38:41]
	v_mfma_i32_16x16x64_i8 v[34:37], v[236:239], v[186:189], v[34:37]
	v_mfma_i32_16x16x64_i8 v[22:25], v[228:231], v[194:197], v[22:25]
	v_mfma_i32_16x16x64_i8 v[18:21], v[236:239], v[194:197], v[18:21]
	v_mfma_i32_16x16x64_i8 v[6:9], v[228:231], v[220:223], v[6:9]
	v_mfma_i32_16x16x64_i8 v[2:5], v[236:239], v[220:223], v[2:5]
	s_setprio 0
	s_add_i32 s95, 0, 0x18000
	v_add_u32_e32 v130, s95, v163
	s_barrier
	ds_read_b128 v[106:109], v130
	ds_read_b128 v[110:113], v130 offset:1024
	ds_read_b128 v[126:129], v130 offset:2048
	ds_read_b128 v[130:133], v130 offset:3072
	s_add_u32 s70, s70, 0x80000
	s_addc_u32 s71, s71, 0
	s_mov_b32 m0, s77
	ds_read_b128 v[146:149], v214 offset:32768
	ds_read_b128 v[178:181], v214 offset:33792
	ds_read_b128 v[182:185], v214 offset:34816
	ds_read_b128 v[186:189], v214 offset:35840
	ds_read_b128 v[190:193], v214 offset:36864
	ds_read_b128 v[194:197], v214 offset:37888
	ds_read_b128 v[198:201], v214 offset:38912
	ds_read_b128 v[220:223], v214 offset:39936
	global_load_lds_dwordx4 v150, s[70:71]
	s_mov_b64 s[96:97], s[70:71]
	s_waitcnt lgkmcnt(8)
	s_barrier
	s_waitcnt lgkmcnt(0)
	s_setprio 1
	s_waitcnt lgkmcnt(0)
	v_mfma_i32_16x16x64_i8 v[142:145], v[106:109], v[146:149], v[142:145]
	v_mfma_i32_16x16x64_i8 v[138:141], v[126:129], v[146:149], v[138:141]
	v_mfma_i32_16x16x64_i8 v[118:121], v[106:109], v[182:185], v[118:121]
	v_mfma_i32_16x16x64_i8 v[114:117], v[126:129], v[182:185], v[114:117]
	v_mfma_i32_16x16x64_i8 v[94:97], v[106:109], v[190:193], v[94:97]
	v_mfma_i32_16x16x64_i8 v[90:93], v[126:129], v[190:193], v[90:93]
	v_mfma_i32_16x16x64_i8 v[78:81], v[106:109], v[198:201], v[78:81]
	v_mfma_i32_16x16x64_i8 v[74:77], v[126:129], v[198:201], v[74:77]
	v_mfma_i32_16x16x64_i8 v[142:145], v[110:113], v[178:181], v[142:145]
	v_mfma_i32_16x16x64_i8 v[138:141], v[130:133], v[178:181], v[138:141]
	v_mfma_i32_16x16x64_i8 v[118:121], v[110:113], v[186:189], v[118:121]
	v_mfma_i32_16x16x64_i8 v[114:117], v[130:133], v[186:189], v[114:117]
	v_mfma_i32_16x16x64_i8 v[94:97], v[110:113], v[194:197], v[94:97]
	v_mfma_i32_16x16x64_i8 v[90:93], v[130:133], v[194:197], v[90:93]
	v_mfma_i32_16x16x64_i8 v[78:81], v[110:113], v[220:223], v[78:81]
	v_mfma_i32_16x16x64_i8 v[74:77], v[130:133], v[220:223], v[74:77]
	s_setprio 0
	s_barrier
	s_add_i32 s70, 0, 0x1c000
	s_add_i32 s71, s95, s75
	v_add_u32_e32 v158, s70, v163
	s_add_u32 s100, s68, 0x80
	s_addc_u32 s101, s69, 0
	s_mov_b32 m0, s71
	ds_read_b128 v[224:227], v158
	ds_read_b128 v[228:231], v158 offset:1024
	ds_read_b128 v[232:235], v158 offset:2048
	ds_read_b128 v[236:239], v158 offset:3072
	global_load_lds_dwordx4 v152, s[100:101]
	s_add_i32 m0, s71, 0x2000
	s_nop 0
	global_load_lds_dwordx4 v156, s[100:101]
	s_waitcnt vmcnt(3)
	s_barrier
	s_waitcnt lgkmcnt(0)
	s_setprio 1
	s_waitcnt lgkmcnt(0)
	v_mfma_i32_16x16x64_i8 v[134:137], v[224:227], v[146:149], v[134:137]
	v_mfma_i32_16x16x64_i8 v[122:125], v[232:235], v[146:149], v[122:125]
	v_mfma_i32_16x16x64_i8 v[102:105], v[224:227], v[182:185], v[102:105]
	v_mfma_i32_16x16x64_i8 v[98:101], v[232:235], v[182:185], v[98:101]
	v_mfma_i32_16x16x64_i8 v[86:89], v[224:227], v[190:193], v[86:89]
	v_mfma_i32_16x16x64_i8 v[82:85], v[232:235], v[190:193], v[82:85]
	v_mfma_i32_16x16x64_i8 v[70:73], v[224:227], v[198:201], v[70:73]
	v_mfma_i32_16x16x64_i8 v[66:69], v[232:235], v[198:201], v[66:69]
	v_mfma_i32_16x16x64_i8 v[134:137], v[228:231], v[178:181], v[134:137]
	v_mfma_i32_16x16x64_i8 v[122:125], v[236:239], v[178:181], v[122:125]
	v_mfma_i32_16x16x64_i8 v[102:105], v[228:231], v[186:189], v[102:105]
	v_mfma_i32_16x16x64_i8 v[98:101], v[236:239], v[186:189], v[98:101]
	v_mfma_i32_16x16x64_i8 v[86:89], v[228:231], v[194:197], v[86:89]
	v_mfma_i32_16x16x64_i8 v[82:85], v[236:239], v[194:197], v[82:85]
	v_mfma_i32_16x16x64_i8 v[70:73], v[228:231], v[220:223], v[70:73]
	v_mfma_i32_16x16x64_i8 v[66:69], v[236:239], v[220:223], v[66:69]
	s_setprio 0
	s_mov_b32 m0, s85
	s_barrier
	ds_read_b128 v[146:149], v214 offset:49152
	ds_read_b128 v[178:181], v214 offset:50176
	ds_read_b128 v[182:185], v214 offset:51200
	ds_read_b128 v[186:189], v214 offset:52224
	ds_read_b128 v[190:193], v214 offset:53248
	ds_read_b128 v[194:197], v214 offset:54272
	ds_read_b128 v[198:201], v214 offset:55296
	ds_read_b128 v[220:223], v214 offset:56320
	global_load_lds_dwordx4 v150, s[98:99]
	s_mov_b32 m0, s86
	s_nop 0
	global_load_lds_dwordx4 v154, s[98:99]
	s_barrier
	s_waitcnt lgkmcnt(0)
	s_setprio 1
	s_waitcnt lgkmcnt(0)
	v_mfma_i32_16x16x64_i8 v[62:65], v[106:109], v[146:149], v[62:65]
	v_mfma_i32_16x16x64_i8 v[58:61], v[126:129], v[146:149], v[58:61]
	v_mfma_i32_16x16x64_i8 v[46:49], v[106:109], v[182:185], v[46:49]
	v_mfma_i32_16x16x64_i8 v[42:45], v[126:129], v[182:185], v[42:45]
	v_mfma_i32_16x16x64_i8 v[30:33], v[106:109], v[190:193], v[30:33]
	v_mfma_i32_16x16x64_i8 v[26:29], v[126:129], v[190:193], v[26:29]
	v_mfma_i32_16x16x64_i8 v[14:17], v[106:109], v[198:201], v[14:17]
	v_mfma_i32_16x16x64_i8 v[10:13], v[126:129], v[198:201], v[10:13]
	v_mfma_i32_16x16x64_i8 v[62:65], v[110:113], v[178:181], v[62:65]
	v_mfma_i32_16x16x64_i8 v[58:61], v[130:133], v[178:181], v[58:61]
	v_mfma_i32_16x16x64_i8 v[46:49], v[110:113], v[186:189], v[46:49]
	v_mfma_i32_16x16x64_i8 v[42:45], v[130:133], v[186:189], v[42:45]
	v_mfma_i32_16x16x64_i8 v[30:33], v[110:113], v[194:197], v[30:33]
	v_mfma_i32_16x16x64_i8 v[26:29], v[130:133], v[194:197], v[26:29]
	v_mfma_i32_16x16x64_i8 v[14:17], v[110:113], v[220:223], v[14:17]
	v_mfma_i32_16x16x64_i8 v[10:13], v[130:133], v[220:223], v[10:13]
	s_setprio 0
	s_barrier
	s_add_u32 s68, s68, 0x80080
	s_addc_u32 s69, s69, 0
	s_add_i32 s70, s70, s75
	s_mov_b32 m0, s70
	s_nop 0
	global_load_lds_dwordx4 v152, s[68:69]
	s_add_i32 m0, s70, 0x2000
	s_nop 0
	global_load_lds_dwordx4 v156, s[68:69]
	s_mov_b32 m0, s78
	s_nop 0
	global_load_lds_dwordx4 v154, s[96:97]
	s_waitcnt vmcnt(7)
	s_barrier
	s_setprio 1
	v_mfma_i32_16x16x64_i8 v[54:57], v[224:227], v[146:149], v[54:57]
	v_mfma_i32_16x16x64_i8 v[50:53], v[232:235], v[146:149], v[50:53]
	v_mfma_i32_16x16x64_i8 v[38:41], v[224:227], v[182:185], v[38:41]
	v_mfma_i32_16x16x64_i8 v[34:37], v[232:235], v[182:185], v[34:37]
	v_mfma_i32_16x16x64_i8 v[22:25], v[224:227], v[190:193], v[22:25]
	v_mfma_i32_16x16x64_i8 v[18:21], v[232:235], v[190:193], v[18:21]
	v_mfma_i32_16x16x64_i8 v[6:9], v[224:227], v[198:201], v[6:9]
	v_mfma_i32_16x16x64_i8 v[2:5], v[232:235], v[198:201], v[2:5]
	v_mfma_i32_16x16x64_i8 v[54:57], v[228:231], v[178:181], v[54:57]
	v_mfma_i32_16x16x64_i8 v[50:53], v[236:239], v[178:181], v[50:53]
	v_mfma_i32_16x16x64_i8 v[38:41], v[228:231], v[186:189], v[38:41]
	v_mfma_i32_16x16x64_i8 v[34:37], v[236:239], v[186:189], v[34:37]
	v_mfma_i32_16x16x64_i8 v[22:25], v[228:231], v[194:197], v[22:25]
	v_mfma_i32_16x16x64_i8 v[18:21], v[236:239], v[194:197], v[18:21]
	v_mfma_i32_16x16x64_i8 v[6:9], v[228:231], v[220:223], v[6:9]
	v_mfma_i32_16x16x64_i8 v[2:5], v[236:239], v[220:223], v[2:5]
	s_setprio 0
	s_add_i32 s94, s94, 2
	s_add_u32 s66, s66, 0x100
	s_addc_u32 s67, s67, 0
	s_add_u32 s92, s92, 0x100
	s_addc_u32 s93, s93, 0
	s_cmp_gt_u32 s94, 29
	s_barrier
	s_cbranch_scc0 .LBB0_301
	s_and_b64 vcc, exec, s[36:37]
	s_cbranch_vccz .LBB0_304
	s_barrier
